# static wave priority in MoBA attention unit: waves 4-7 at s_setprio 2 for the unit, reset at unit end (on v16)
# baseline (speedup 1.0000x reference)
.LBB0_608:
	s_or_b64 exec, exec, s[28:29]
	v_add_u32_e32 v74, s50, v198
	s_waitcnt lgkmcnt(0)
	ds_read_b128 v[66:69], v74
	ds_read_b128 v[70:73], v74 offset:32
	s_lshl_b32 s13, s13, 5
	s_add_i32 s14, s13, s74
	s_ashr_i32 s15, s14, 31
	s_lshl_b64 s[14:15], s[14:15], 15
	s_waitcnt lgkmcnt(0)
	v_rcp_f32_e32 v75, v66
	v_lshlrev_b32_e32 v85, 6, v1
	s_add_u32 s14, s4, s14
	s_mulk_i32 s75, 0x1200
	v_and_b32_e32 v114, 64, v85
	v_lshrrev_b32_e32 v85, 3, v1
	s_addc_u32 s15, s5, s15
	v_rcp_f32_e32 v76, v67
	s_add_i32 s13, s75, 0
	v_bfe_u32 v84, v1, 1, 5
	v_and_b32_e32 v85, 4, v85
	v_lshlrev_b32_e32 v1, 1, v1
	s_add_i32 s13, s13, 0x16000
	v_and_b32_e32 v1, 62, v1
	v_mul_u32_u24_e32 v85, 0x90, v85
	v_mul_f32_e32 v50, v50, v75
	v_add3_u32 v1, s13, v85, v1
	v_mul_f32_e32 v34, v34, v75
	v_rcp_f32_e32 v77, v68
	v_rcp_f32_e32 v78, v69
	v_rcp_f32_e32 v79, v70
	ds_read_b128 v[66:69], v74 offset:64
	v_rcp_f32_e32 v80, v71
	v_rcp_f32_e32 v81, v72
	v_rcp_f32_e32 v82, v73
	ds_read_b128 v[70:73], v74 offset:96
	v_cvt_pk_bf16_f32 v50, v50, v115
	ds_write_b16 v1, v50
	v_cvt_pk_bf16_f32 v34, v34, v115
	ds_write_b16 v1, v34 offset:64
	v_mul_f32_e32 v34, v51, v76
	v_cvt_pk_bf16_f32 v34, v34, v115
	ds_write_b16 v1, v34 offset:144
	v_mul_f32_e32 v34, v35, v76
	v_cvt_pk_bf16_f32 v34, v34, v115
	ds_write_b16 v1, v34 offset:208
	v_mul_f32_e32 v34, v52, v77
	v_cvt_pk_bf16_f32 v34, v34, v115
	ds_write_b16 v1, v34 offset:288
	v_mul_f32_e32 v34, v36, v77
	v_cvt_pk_bf16_f32 v34, v34, v115
	ds_write_b16 v1, v34 offset:352
	v_mul_f32_e32 v34, v53, v78
	v_cvt_pk_bf16_f32 v34, v34, v115
	ds_write_b16 v1, v34 offset:432
	v_mul_f32_e32 v34, v37, v78
	v_cvt_pk_bf16_f32 v34, v34, v115
	ds_write_b16 v1, v34 offset:496
	v_mul_f32_e32 v34, v54, v79
	v_cvt_pk_bf16_f32 v34, v34, v115
	ds_write_b16 v1, v34 offset:1152
	v_mul_f32_e32 v34, v38, v79
	v_cvt_pk_bf16_f32 v34, v34, v115
	ds_write_b16 v1, v34 offset:1216
	v_mul_f32_e32 v34, v55, v80
	v_cvt_pk_bf16_f32 v34, v34, v115
	ds_write_b16 v1, v34 offset:1296
	v_mul_f32_e32 v34, v39, v80
	v_cvt_pk_bf16_f32 v34, v34, v115
	ds_write_b16 v1, v34 offset:1360
	v_mul_f32_e32 v34, v56, v81
	v_cvt_pk_bf16_f32 v34, v34, v115
	ds_write_b16 v1, v34 offset:1440
	v_mul_f32_e32 v34, v40, v81
	v_cvt_pk_bf16_f32 v34, v34, v115
	s_waitcnt lgkmcnt(0)
	v_rcp_f32_e32 v74, v66
	ds_write_b16 v1, v34 offset:1504
	v_mul_f32_e32 v34, v57, v82
	v_cvt_pk_bf16_f32 v34, v34, v115
	ds_write_b16 v1, v34 offset:1584
	v_mul_f32_e32 v34, v41, v82
	v_cvt_pk_bf16_f32 v34, v34, v115
	v_rcp_f32_e32 v83, v67
	ds_write_b16 v1, v34 offset:1648
	v_mul_f32_e32 v34, v58, v74
	v_cvt_pk_bf16_f32 v34, v34, v115
	ds_write_b16 v1, v34 offset:2304
	v_mul_f32_e32 v34, v42, v74
	v_cvt_pk_bf16_f32 v34, v34, v115
	v_rcp_f32_e32 v68, v68
	ds_write_b16 v1, v34 offset:2368
	v_mul_f32_e32 v34, v59, v83
	v_cvt_pk_bf16_f32 v34, v34, v115
	ds_write_b16 v1, v34 offset:2448
	v_mul_f32_e32 v34, v43, v83
	v_cvt_pk_bf16_f32 v34, v34, v115
	v_rcp_f32_e32 v69, v69
	ds_write_b16 v1, v34 offset:2512
	v_mul_f32_e32 v34, v60, v68
	v_cvt_pk_bf16_f32 v34, v34, v115
	ds_write_b16 v1, v34 offset:2592
	v_mul_f32_e32 v34, v44, v68
	v_cvt_pk_bf16_f32 v34, v34, v115
	v_rcp_f32_e32 v70, v70
	ds_write_b16 v1, v34 offset:2656
	v_mul_f32_e32 v34, v61, v69
	v_cvt_pk_bf16_f32 v34, v34, v115
	ds_write_b16 v1, v34 offset:2736
	v_mul_f32_e32 v34, v45, v69
	v_cvt_pk_bf16_f32 v34, v34, v115
	v_rcp_f32_e32 v71, v71
	ds_write_b16 v1, v34 offset:2800
	v_mul_f32_e32 v34, v62, v70
	v_cvt_pk_bf16_f32 v34, v34, v115
	ds_write_b16 v1, v34 offset:3456
	v_mul_f32_e32 v34, v46, v70
	v_cvt_pk_bf16_f32 v34, v34, v115
	v_rcp_f32_e32 v72, v72
	ds_write_b16 v1, v34 offset:3520
	v_mul_f32_e32 v34, v63, v71
	v_cvt_pk_bf16_f32 v34, v34, v115
	ds_write_b16 v1, v34 offset:3600
	v_mul_f32_e32 v34, v47, v71
	v_cvt_pk_bf16_f32 v34, v34, v115
	v_rcp_f32_e32 v73, v73
	ds_write_b16 v1, v34 offset:3664
	v_mul_f32_e32 v34, v64, v72
	v_cvt_pk_bf16_f32 v34, v34, v115
	ds_write_b16 v1, v34 offset:3744
	v_mul_f32_e32 v34, v48, v72
	v_cvt_pk_bf16_f32 v34, v34, v115
	ds_write_b16 v1, v34 offset:3808
	v_mul_f32_e32 v34, v65, v73
	v_cvt_pk_bf16_f32 v34, v34, v115
	ds_write_b16 v1, v34 offset:3888
	v_mul_f32_e32 v34, v49, v73
	v_or_b32_e32 v66, s12, v84
	v_mul_u32_u24_e32 v84, 0x90, v84
	v_cvt_pk_bf16_f32 v34, v34, v115
	ds_write_b16 v1, v34 offset:3952
	v_add3_u32 v84, s13, v84, v114
	s_waitcnt lgkmcnt(0)
	ds_read_b128 v[34:37], v84
	ds_read_b128 v[38:41], v84 offset:16
	ds_read_b128 v[42:45], v84 offset:32
	ds_read_b128 v[46:49], v84 offset:48
	v_ashrrev_i32_e32 v67, 31, v66
	v_lshlrev_b64 v[66:67], 7, v[66:67]
	v_lshl_add_u64 v[66:67], s[14:15], 0, v[66:67]
	v_lshl_add_u64 v[66:67], v[66:67], 0, v[114:115]
	v_mul_f32_e32 v18, v18, v75
	v_mul_f32_e32 v2, v2, v75
	s_waitcnt lgkmcnt(0)
	s_waitcnt lgkmcnt(0)
	global_store_dwordx4 v[66:67], v[34:37], off
	global_store_dwordx4 v[66:67], v[38:41], off offset:16
	global_store_dwordx4 v[66:67], v[42:45], off offset:32
	global_store_dwordx4 v[66:67], v[46:49], off offset:48
	v_cvt_pk_bf16_f32 v18, v18, v115
	ds_write_b16 v1, v18
	v_cvt_pk_bf16_f32 v2, v2, v115
	ds_write_b16 v1, v2 offset:64
	v_mul_f32_e32 v2, v19, v76
	v_cvt_pk_bf16_f32 v2, v2, v115
	ds_write_b16 v1, v2 offset:144
	v_mul_f32_e32 v2, v3, v76
	v_cvt_pk_bf16_f32 v2, v2, v115
	ds_write_b16 v1, v2 offset:208
	v_mul_f32_e32 v2, v20, v77
	v_cvt_pk_bf16_f32 v2, v2, v115
	ds_write_b16 v1, v2 offset:288
	v_mul_f32_e32 v2, v4, v77
	v_cvt_pk_bf16_f32 v2, v2, v115
	ds_write_b16 v1, v2 offset:352
	v_mul_f32_e32 v2, v21, v78
	v_cvt_pk_bf16_f32 v2, v2, v115
	ds_write_b16 v1, v2 offset:432
	v_mul_f32_e32 v2, v5, v78
	v_cvt_pk_bf16_f32 v2, v2, v115
	ds_write_b16 v1, v2 offset:496
	v_mul_f32_e32 v2, v22, v79
	v_cvt_pk_bf16_f32 v2, v2, v115
	ds_write_b16 v1, v2 offset:1152
	v_mul_f32_e32 v2, v6, v79
	v_cvt_pk_bf16_f32 v2, v2, v115
	ds_write_b16 v1, v2 offset:1216
	v_mul_f32_e32 v2, v23, v80
	v_cvt_pk_bf16_f32 v2, v2, v115
	ds_write_b16 v1, v2 offset:1296
	v_mul_f32_e32 v2, v7, v80
	v_cvt_pk_bf16_f32 v2, v2, v115
	ds_write_b16 v1, v2 offset:1360
	v_mul_f32_e32 v2, v24, v81
	v_cvt_pk_bf16_f32 v2, v2, v115
	ds_write_b16 v1, v2 offset:1440
	v_mul_f32_e32 v2, v8, v81
	v_cvt_pk_bf16_f32 v2, v2, v115
	ds_write_b16 v1, v2 offset:1504
	v_mul_f32_e32 v2, v25, v82
	v_cvt_pk_bf16_f32 v2, v2, v115
	ds_write_b16 v1, v2 offset:1584
	v_mul_f32_e32 v2, v9, v82
	v_cvt_pk_bf16_f32 v2, v2, v115
	ds_write_b16 v1, v2 offset:1648
	v_mul_f32_e32 v2, v26, v74
	v_cvt_pk_bf16_f32 v2, v2, v115
	ds_write_b16 v1, v2 offset:2304
	v_mul_f32_e32 v2, v10, v74
	v_cvt_pk_bf16_f32 v2, v2, v115
	ds_write_b16 v1, v2 offset:2368
	v_mul_f32_e32 v2, v27, v83
	v_cvt_pk_bf16_f32 v2, v2, v115
	ds_write_b16 v1, v2 offset:2448
	v_mul_f32_e32 v2, v11, v83
	v_cvt_pk_bf16_f32 v2, v2, v115
	ds_write_b16 v1, v2 offset:2512
	v_mul_f32_e32 v2, v28, v68
	v_cvt_pk_bf16_f32 v2, v2, v115
	ds_write_b16 v1, v2 offset:2592
	v_mul_f32_e32 v2, v12, v68
	v_cvt_pk_bf16_f32 v2, v2, v115
	ds_write_b16 v1, v2 offset:2656
	v_mul_f32_e32 v2, v29, v69
	v_cvt_pk_bf16_f32 v2, v2, v115
	ds_write_b16 v1, v2 offset:2736
	v_mul_f32_e32 v2, v13, v69
	v_cvt_pk_bf16_f32 v2, v2, v115
	ds_write_b16 v1, v2 offset:2800
	v_mul_f32_e32 v2, v30, v70
	v_cvt_pk_bf16_f32 v2, v2, v115
	ds_write_b16 v1, v2 offset:3456
	v_mul_f32_e32 v2, v14, v70
	v_cvt_pk_bf16_f32 v2, v2, v115
	ds_write_b16 v1, v2 offset:3520
	v_mul_f32_e32 v2, v31, v71
	v_cvt_pk_bf16_f32 v2, v2, v115
	ds_write_b16 v1, v2 offset:3600
	v_mul_f32_e32 v2, v15, v71
	v_cvt_pk_bf16_f32 v2, v2, v115
	ds_write_b16 v1, v2 offset:3664
	v_mul_f32_e32 v2, v32, v72
	v_cvt_pk_bf16_f32 v2, v2, v115
	ds_write_b16 v1, v2 offset:3744
	v_mul_f32_e32 v2, v16, v72
	v_cvt_pk_bf16_f32 v2, v2, v115
	ds_write_b16 v1, v2 offset:3808
	v_mul_f32_e32 v2, v33, v73
	v_cvt_pk_bf16_f32 v2, v2, v115
	ds_write_b16 v1, v2 offset:3888
	v_mul_f32_e32 v2, v17, v73
	v_cvt_pk_bf16_f32 v2, v2, v115
	ds_write_b16 v1, v2 offset:3952
	s_waitcnt lgkmcnt(0)
	ds_read_b128 v[2:5], v84
	ds_read_b128 v[6:9], v84 offset:16
	ds_read_b128 v[10:13], v84 offset:32
	ds_read_b128 v[14:17], v84 offset:48
	s_waitcnt lgkmcnt(0)
	v_add_co_u32_e32 v18, vcc, 0x8000, v66
	s_mov_b64 s[68:69], 0
	s_nop 0
	v_addc_co_u32_e32 v19, vcc, 0, v67, vcc
	s_and_b64 vcc, exec, s[0:1]
	s_waitcnt lgkmcnt(0)
	global_store_dwordx4 v[18:19], v[2:5], off
	global_store_dwordx4 v[18:19], v[6:9], off offset:16
	global_store_dwordx4 v[18:19], v[10:13], off offset:32
	global_store_dwordx4 v[18:19], v[14:17], off offset:48
	s_waitcnt vmcnt(0)
	s_setprio 0
	s_barrier
	s_cbranch_vccnz .LBB0_606
.LBB0_609:
	v_readlane_b32 s0, v254, 6
	s_nop 3
	s_cmp_lt_u32 s0, 4
	s_cbranch_scc1 .Lap_lo
	s_setprio 2
